# P4 RG gate epilogue hand-written: packed f32 add/mul for the sigmoid chains and i*x, all loads up front, saddr addressing (same per-element operations)
# speedup vs baseline: 1.0047x; 1.0026x over previous
.LBB0_640:
	s_and_b32 s98, s12, 1
	s_lshl_b32 s99, s12, 6
	s_and_b32 s99, s99, 0xffffff80
	s_or_b32 s99, s99, s63
	v_lshl_add_u32 v251, v183, 3, s99
	v_lshlrev_b32_e32 v250, 2, v251
	v_lshlrev_b32_e32 v251, 1, v251
	v_lshl_add_u32 v251, v182, 11, v251
	s_lshl_b32 s28, s98, 12
	s_add_u32 s100, s8, s28
	s_addc_u32 s101, s9, 0
	global_load_dwordx4 v[142:145], v250, s[100:101]
	global_load_dwordx4 v[130:133], v250, s[100:101] offset:16
	s_add_u32 s100, s10, s28
	s_addc_u32 s101, s11, 0
	global_load_dwordx4 v[146:149], v250, s[100:101]
	global_load_dwordx4 v[134:137], v250, s[100:101] offset:16
	s_lshl_b32 s28, s24, 8
	s_add_i32 s28, s28, s62
	s_lshl_b32 s29, s28, 11
	s_add_u32 s100, s4, s29
	s_addc_u32 s101, s5, 0
	global_load_dwordx4 v[204:207], v251, s[100:101]
	v_add_u32_e32 v253, 0x8000, v251
	global_load_dwordx4 v[170:173], v253, s[100:101]
	v_add_u32_e32 v252, 0x10000, v251
	global_load_dwordx4 v[166:169], v252, s[100:101]
	v_add_u32_e32 v253, 0x18000, v251
	global_load_dwordx4 v[162:165], v253, s[100:101]
	v_add_u32_e32 v252, 0x40000, v251
	global_load_dwordx4 v[158:161], v252, s[100:101]
	v_add_u32_e32 v253, 0x48000, v251
	global_load_dwordx4 v[154:157], v253, s[100:101]
	v_add_u32_e32 v252, 0x50000, v251
	global_load_dwordx4 v[150:153], v252, s[100:101]
	v_add_u32_e32 v253, 0x58000, v251
	global_load_dwordx4 v[138:141], v253, s[100:101]
	s_mul_i32 s29, s98, 0x8400
	s_add_i32 s28, s28, s29
	s_lshl_b32 s28, s28, 11
	s_add_u32 s98, s16, s28
	s_addc_u32 s99, s17, 0
	s_add_u32 s100, s18, s28
	s_addc_u32 s101, s19, 0
	s_mov_b32 s28, 0xbfb8aa3b
	s_waitcnt vmcnt(6)
	v_pk_add_f32 v[126:127], v[126:127], v[142:143]
	v_pk_add_f32 v[128:129], v[128:129], v[144:145]
	v_pk_add_f32 v[118:119], v[118:119], v[130:131]
	v_pk_add_f32 v[120:121], v[120:121], v[132:133]
	v_pk_add_f32 v[122:123], v[122:123], v[146:147]
	v_pk_add_f32 v[124:125], v[124:125], v[148:149]
	v_pk_add_f32 v[114:115], v[114:115], v[134:135]
	v_pk_add_f32 v[116:117], v[116:117], v[136:137]
	v_pk_add_f32 v[110:111], v[110:111], v[142:143]
	v_pk_add_f32 v[112:113], v[112:113], v[144:145]
	v_pk_add_f32 v[102:103], v[102:103], v[130:131]
	v_pk_add_f32 v[104:105], v[104:105], v[132:133]
	v_pk_add_f32 v[106:107], v[106:107], v[146:147]
	v_pk_add_f32 v[108:109], v[108:109], v[148:149]
	v_pk_add_f32 v[98:99], v[98:99], v[134:135]
	v_pk_add_f32 v[100:101], v[100:101], v[136:137]
	v_pk_mul_f32 v[126:127], v[126:127], s[28:29] op_sel_hi:[1,0]
	v_pk_mul_f32 v[128:129], v[128:129], s[28:29] op_sel_hi:[1,0]
	v_pk_mul_f32 v[118:119], v[118:119], s[28:29] op_sel_hi:[1,0]
	v_pk_mul_f32 v[120:121], v[120:121], s[28:29] op_sel_hi:[1,0]
	v_pk_mul_f32 v[122:123], v[122:123], s[28:29] op_sel_hi:[1,0]
	v_pk_mul_f32 v[124:125], v[124:125], s[28:29] op_sel_hi:[1,0]
	v_pk_mul_f32 v[114:115], v[114:115], s[28:29] op_sel_hi:[1,0]
	v_pk_mul_f32 v[116:117], v[116:117], s[28:29] op_sel_hi:[1,0]
	v_pk_mul_f32 v[110:111], v[110:111], s[28:29] op_sel_hi:[1,0]
	v_pk_mul_f32 v[112:113], v[112:113], s[28:29] op_sel_hi:[1,0]
	v_pk_mul_f32 v[102:103], v[102:103], s[28:29] op_sel_hi:[1,0]
	v_pk_mul_f32 v[104:105], v[104:105], s[28:29] op_sel_hi:[1,0]
	v_pk_mul_f32 v[106:107], v[106:107], s[28:29] op_sel_hi:[1,0]
	v_pk_mul_f32 v[108:109], v[108:109], s[28:29] op_sel_hi:[1,0]
	v_pk_mul_f32 v[98:99], v[98:99], s[28:29] op_sel_hi:[1,0]
	v_pk_mul_f32 v[100:101], v[100:101], s[28:29] op_sel_hi:[1,0]
	v_exp_f32_e32 v126, v126
	v_exp_f32_e32 v127, v127
	v_exp_f32_e32 v128, v128
	v_exp_f32_e32 v129, v129
	v_exp_f32_e32 v118, v118
	v_exp_f32_e32 v119, v119
	v_exp_f32_e32 v120, v120
	v_exp_f32_e32 v121, v121
	v_exp_f32_e32 v122, v122
	v_exp_f32_e32 v123, v123
	v_exp_f32_e32 v124, v124
	v_exp_f32_e32 v125, v125
	v_exp_f32_e32 v114, v114
	v_exp_f32_e32 v115, v115
	v_exp_f32_e32 v116, v116
	v_exp_f32_e32 v117, v117
	v_exp_f32_e32 v110, v110
	v_exp_f32_e32 v111, v111
	v_exp_f32_e32 v112, v112
	v_exp_f32_e32 v113, v113
	v_exp_f32_e32 v102, v102
	v_exp_f32_e32 v103, v103
	v_exp_f32_e32 v104, v104
	v_exp_f32_e32 v105, v105
	v_exp_f32_e32 v106, v106
	v_exp_f32_e32 v107, v107
	v_exp_f32_e32 v108, v108
	v_exp_f32_e32 v109, v109
	v_exp_f32_e32 v98, v98
	v_exp_f32_e32 v99, v99
	v_exp_f32_e32 v100, v100
	v_exp_f32_e32 v101, v101
	v_pk_add_f32 v[126:127], v[126:127], 1.0 op_sel_hi:[1,0]
	v_pk_add_f32 v[128:129], v[128:129], 1.0 op_sel_hi:[1,0]
	v_pk_add_f32 v[118:119], v[118:119], 1.0 op_sel_hi:[1,0]
	v_pk_add_f32 v[120:121], v[120:121], 1.0 op_sel_hi:[1,0]
	v_pk_add_f32 v[122:123], v[122:123], 1.0 op_sel_hi:[1,0]
	v_pk_add_f32 v[124:125], v[124:125], 1.0 op_sel_hi:[1,0]
	v_pk_add_f32 v[114:115], v[114:115], 1.0 op_sel_hi:[1,0]
	v_pk_add_f32 v[116:117], v[116:117], 1.0 op_sel_hi:[1,0]
	v_pk_add_f32 v[110:111], v[110:111], 1.0 op_sel_hi:[1,0]
	v_pk_add_f32 v[112:113], v[112:113], 1.0 op_sel_hi:[1,0]
	v_pk_add_f32 v[102:103], v[102:103], 1.0 op_sel_hi:[1,0]
	v_pk_add_f32 v[104:105], v[104:105], 1.0 op_sel_hi:[1,0]
	v_pk_add_f32 v[106:107], v[106:107], 1.0 op_sel_hi:[1,0]
	v_pk_add_f32 v[108:109], v[108:109], 1.0 op_sel_hi:[1,0]
	v_pk_add_f32 v[98:99], v[98:99], 1.0 op_sel_hi:[1,0]
	v_pk_add_f32 v[100:101], v[100:101], 1.0 op_sel_hi:[1,0]
	v_rcp_f32_e32 v126, v126
	v_rcp_f32_e32 v127, v127
	v_rcp_f32_e32 v128, v128
	v_rcp_f32_e32 v129, v129
	v_rcp_f32_e32 v118, v118
	v_rcp_f32_e32 v119, v119
	v_rcp_f32_e32 v120, v120
	v_rcp_f32_e32 v121, v121
	v_rcp_f32_e32 v122, v122
	v_rcp_f32_e32 v123, v123
	v_rcp_f32_e32 v124, v124
	v_rcp_f32_e32 v125, v125
	v_rcp_f32_e32 v114, v114
	v_rcp_f32_e32 v115, v115
	v_rcp_f32_e32 v116, v116
	v_rcp_f32_e32 v117, v117
	v_rcp_f32_e32 v110, v110
	v_rcp_f32_e32 v111, v111
	v_rcp_f32_e32 v112, v112
	v_rcp_f32_e32 v113, v113
	v_rcp_f32_e32 v102, v102
	v_rcp_f32_e32 v103, v103
	v_rcp_f32_e32 v104, v104
	v_rcp_f32_e32 v105, v105
	v_rcp_f32_e32 v106, v106
	v_rcp_f32_e32 v107, v107
	v_rcp_f32_e32 v108, v108
	v_rcp_f32_e32 v109, v109
	v_rcp_f32_e32 v98, v98
	v_rcp_f32_e32 v99, v99
	v_rcp_f32_e32 v100, v100
	v_rcp_f32_e32 v101, v101
	v_lshlrev_b32_e32 v214, 16, v204
	v_and_b32_e32 v215, 0xffff0000, v204
	v_lshlrev_b32_e32 v216, 16, v205
	v_and_b32_e32 v217, 0xffff0000, v205
	v_lshlrev_b32_e32 v218, 16, v206
	v_and_b32_e32 v219, 0xffff0000, v206
	v_lshlrev_b32_e32 v220, 16, v207
	v_and_b32_e32 v221, 0xffff0000, v207
	v_lshlrev_b32_e32 v222, 16, v170
	v_and_b32_e32 v223, 0xffff0000, v170
	v_lshlrev_b32_e32 v224, 16, v171
	v_and_b32_e32 v225, 0xffff0000, v171
	v_lshlrev_b32_e32 v226, 16, v172
	v_and_b32_e32 v227, 0xffff0000, v172
	v_lshlrev_b32_e32 v228, 16, v173
	v_and_b32_e32 v229, 0xffff0000, v173
	v_pk_mul_f32 v[122:123], v[122:123], v[214:215]
	v_pk_mul_f32 v[124:125], v[124:125], v[216:217]
	v_pk_mul_f32 v[114:115], v[114:115], v[218:219]
	v_pk_mul_f32 v[116:117], v[116:117], v[220:221]
	v_pk_mul_f32 v[106:107], v[106:107], v[222:223]
	v_pk_mul_f32 v[108:109], v[108:109], v[224:225]
	v_pk_mul_f32 v[98:99], v[98:99], v[226:227]
	v_pk_mul_f32 v[100:101], v[100:101], v[228:229]
	v_cvt_pk_bf16_f32 v234, v126, v127
	v_cvt_pk_bf16_f32 v235, v128, v129
	v_cvt_pk_bf16_f32 v236, v118, v119
	v_cvt_pk_bf16_f32 v237, v120, v121
	v_cvt_pk_bf16_f32 v238, v122, v123
	v_cvt_pk_bf16_f32 v239, v124, v125
	v_cvt_pk_bf16_f32 v240, v114, v115
	v_cvt_pk_bf16_f32 v241, v116, v117
	v_cvt_pk_bf16_f32 v242, v110, v111
	v_cvt_pk_bf16_f32 v243, v112, v113
	v_cvt_pk_bf16_f32 v244, v102, v103
	v_cvt_pk_bf16_f32 v245, v104, v105
	v_cvt_pk_bf16_f32 v246, v106, v107
	v_cvt_pk_bf16_f32 v247, v108, v109
	v_cvt_pk_bf16_f32 v248, v98, v99
	v_cvt_pk_bf16_f32 v249, v100, v101
	v_add_u32_e32 v253, 0x8000, v251
	global_store_dwordx4 v251, v[234:237], s[98:99]
	global_store_dwordx4 v251, v[238:241], s[100:101]
	global_store_dwordx4 v253, v[242:245], s[98:99]
	global_store_dwordx4 v253, v[246:249], s[100:101]
	s_waitcnt vmcnt(8)
	v_pk_add_f32 v[94:95], v[94:95], v[142:143]
	v_pk_add_f32 v[96:97], v[96:97], v[144:145]
	v_pk_add_f32 v[86:87], v[86:87], v[130:131]
	v_pk_add_f32 v[88:89], v[88:89], v[132:133]
	v_pk_add_f32 v[90:91], v[90:91], v[146:147]
	v_pk_add_f32 v[92:93], v[92:93], v[148:149]
	v_pk_add_f32 v[82:83], v[82:83], v[134:135]
	v_pk_add_f32 v[84:85], v[84:85], v[136:137]
	v_pk_add_f32 v[78:79], v[78:79], v[142:143]
	v_pk_add_f32 v[80:81], v[80:81], v[144:145]
	v_pk_add_f32 v[70:71], v[70:71], v[130:131]
	v_pk_add_f32 v[72:73], v[72:73], v[132:133]
	v_pk_add_f32 v[74:75], v[74:75], v[146:147]
	v_pk_add_f32 v[76:77], v[76:77], v[148:149]
	v_pk_add_f32 v[66:67], v[66:67], v[134:135]
	v_pk_add_f32 v[68:69], v[68:69], v[136:137]
	v_pk_mul_f32 v[94:95], v[94:95], s[28:29] op_sel_hi:[1,0]
	v_pk_mul_f32 v[96:97], v[96:97], s[28:29] op_sel_hi:[1,0]
	v_pk_mul_f32 v[86:87], v[86:87], s[28:29] op_sel_hi:[1,0]
	v_pk_mul_f32 v[88:89], v[88:89], s[28:29] op_sel_hi:[1,0]
	v_pk_mul_f32 v[90:91], v[90:91], s[28:29] op_sel_hi:[1,0]
	v_pk_mul_f32 v[92:93], v[92:93], s[28:29] op_sel_hi:[1,0]
	v_pk_mul_f32 v[82:83], v[82:83], s[28:29] op_sel_hi:[1,0]
	v_pk_mul_f32 v[84:85], v[84:85], s[28:29] op_sel_hi:[1,0]
	v_pk_mul_f32 v[78:79], v[78:79], s[28:29] op_sel_hi:[1,0]
	v_pk_mul_f32 v[80:81], v[80:81], s[28:29] op_sel_hi:[1,0]
	v_pk_mul_f32 v[70:71], v[70:71], s[28:29] op_sel_hi:[1,0]
	v_pk_mul_f32 v[72:73], v[72:73], s[28:29] op_sel_hi:[1,0]
	v_pk_mul_f32 v[74:75], v[74:75], s[28:29] op_sel_hi:[1,0]
	v_pk_mul_f32 v[76:77], v[76:77], s[28:29] op_sel_hi:[1,0]
	v_pk_mul_f32 v[66:67], v[66:67], s[28:29] op_sel_hi:[1,0]
	v_pk_mul_f32 v[68:69], v[68:69], s[28:29] op_sel_hi:[1,0]
	v_exp_f32_e32 v94, v94
	v_exp_f32_e32 v95, v95
	v_exp_f32_e32 v96, v96
	v_exp_f32_e32 v97, v97
	v_exp_f32_e32 v86, v86
	v_exp_f32_e32 v87, v87
	v_exp_f32_e32 v88, v88
	v_exp_f32_e32 v89, v89
	v_exp_f32_e32 v90, v90
	v_exp_f32_e32 v91, v91
	v_exp_f32_e32 v92, v92
	v_exp_f32_e32 v93, v93
	v_exp_f32_e32 v82, v82
	v_exp_f32_e32 v83, v83
	v_exp_f32_e32 v84, v84
	v_exp_f32_e32 v85, v85
	v_exp_f32_e32 v78, v78
	v_exp_f32_e32 v79, v79
	v_exp_f32_e32 v80, v80
	v_exp_f32_e32 v81, v81
	v_exp_f32_e32 v70, v70
	v_exp_f32_e32 v71, v71
	v_exp_f32_e32 v72, v72
	v_exp_f32_e32 v73, v73
	v_exp_f32_e32 v74, v74
	v_exp_f32_e32 v75, v75
	v_exp_f32_e32 v76, v76
	v_exp_f32_e32 v77, v77
	v_exp_f32_e32 v66, v66
	v_exp_f32_e32 v67, v67
	v_exp_f32_e32 v68, v68
	v_exp_f32_e32 v69, v69
	v_pk_add_f32 v[94:95], v[94:95], 1.0 op_sel_hi:[1,0]
	v_pk_add_f32 v[96:97], v[96:97], 1.0 op_sel_hi:[1,0]
	v_pk_add_f32 v[86:87], v[86:87], 1.0 op_sel_hi:[1,0]
	v_pk_add_f32 v[88:89], v[88:89], 1.0 op_sel_hi:[1,0]
	v_pk_add_f32 v[90:91], v[90:91], 1.0 op_sel_hi:[1,0]
	v_pk_add_f32 v[92:93], v[92:93], 1.0 op_sel_hi:[1,0]
	v_pk_add_f32 v[82:83], v[82:83], 1.0 op_sel_hi:[1,0]
	v_pk_add_f32 v[84:85], v[84:85], 1.0 op_sel_hi:[1,0]
	v_pk_add_f32 v[78:79], v[78:79], 1.0 op_sel_hi:[1,0]
	v_pk_add_f32 v[80:81], v[80:81], 1.0 op_sel_hi:[1,0]
	v_pk_add_f32 v[70:71], v[70:71], 1.0 op_sel_hi:[1,0]
	v_pk_add_f32 v[72:73], v[72:73], 1.0 op_sel_hi:[1,0]
	v_pk_add_f32 v[74:75], v[74:75], 1.0 op_sel_hi:[1,0]
	v_pk_add_f32 v[76:77], v[76:77], 1.0 op_sel_hi:[1,0]
	v_pk_add_f32 v[66:67], v[66:67], 1.0 op_sel_hi:[1,0]
	v_pk_add_f32 v[68:69], v[68:69], 1.0 op_sel_hi:[1,0]
	v_rcp_f32_e32 v94, v94
	v_rcp_f32_e32 v95, v95
	v_rcp_f32_e32 v96, v96
	v_rcp_f32_e32 v97, v97
	v_rcp_f32_e32 v86, v86
	v_rcp_f32_e32 v87, v87
	v_rcp_f32_e32 v88, v88
	v_rcp_f32_e32 v89, v89
	v_rcp_f32_e32 v90, v90
	v_rcp_f32_e32 v91, v91
	v_rcp_f32_e32 v92, v92
	v_rcp_f32_e32 v93, v93
	v_rcp_f32_e32 v82, v82
	v_rcp_f32_e32 v83, v83
	v_rcp_f32_e32 v84, v84
	v_rcp_f32_e32 v85, v85
	v_rcp_f32_e32 v78, v78
	v_rcp_f32_e32 v79, v79
	v_rcp_f32_e32 v80, v80
	v_rcp_f32_e32 v81, v81
	v_rcp_f32_e32 v70, v70
	v_rcp_f32_e32 v71, v71
	v_rcp_f32_e32 v72, v72
	v_rcp_f32_e32 v73, v73
	v_rcp_f32_e32 v74, v74
	v_rcp_f32_e32 v75, v75
	v_rcp_f32_e32 v76, v76
	v_rcp_f32_e32 v77, v77
	v_rcp_f32_e32 v66, v66
	v_rcp_f32_e32 v67, v67
	v_rcp_f32_e32 v68, v68
	v_rcp_f32_e32 v69, v69
	v_lshlrev_b32_e32 v214, 16, v166
	v_and_b32_e32 v215, 0xffff0000, v166
	v_lshlrev_b32_e32 v216, 16, v167
	v_and_b32_e32 v217, 0xffff0000, v167
	v_lshlrev_b32_e32 v218, 16, v168
	v_and_b32_e32 v219, 0xffff0000, v168
	v_lshlrev_b32_e32 v220, 16, v169
	v_and_b32_e32 v221, 0xffff0000, v169
	v_lshlrev_b32_e32 v222, 16, v162
	v_and_b32_e32 v223, 0xffff0000, v162
	v_lshlrev_b32_e32 v224, 16, v163
	v_and_b32_e32 v225, 0xffff0000, v163
	v_lshlrev_b32_e32 v226, 16, v164
	v_and_b32_e32 v227, 0xffff0000, v164
	v_lshlrev_b32_e32 v228, 16, v165
	v_and_b32_e32 v229, 0xffff0000, v165
	v_pk_mul_f32 v[90:91], v[90:91], v[214:215]
	v_pk_mul_f32 v[92:93], v[92:93], v[216:217]
	v_pk_mul_f32 v[82:83], v[82:83], v[218:219]
	v_pk_mul_f32 v[84:85], v[84:85], v[220:221]
	v_pk_mul_f32 v[74:75], v[74:75], v[222:223]
	v_pk_mul_f32 v[76:77], v[76:77], v[224:225]
	v_pk_mul_f32 v[66:67], v[66:67], v[226:227]
	v_pk_mul_f32 v[68:69], v[68:69], v[228:229]
	v_cvt_pk_bf16_f32 v234, v94, v95
	v_cvt_pk_bf16_f32 v235, v96, v97
	v_cvt_pk_bf16_f32 v236, v86, v87
	v_cvt_pk_bf16_f32 v237, v88, v89
	v_cvt_pk_bf16_f32 v238, v90, v91
	v_cvt_pk_bf16_f32 v239, v92, v93
	v_cvt_pk_bf16_f32 v240, v82, v83
	v_cvt_pk_bf16_f32 v241, v84, v85
	v_cvt_pk_bf16_f32 v242, v78, v79
	v_cvt_pk_bf16_f32 v243, v80, v81
	v_cvt_pk_bf16_f32 v244, v70, v71
	v_cvt_pk_bf16_f32 v245, v72, v73
	v_cvt_pk_bf16_f32 v246, v74, v75
	v_cvt_pk_bf16_f32 v247, v76, v77
	v_cvt_pk_bf16_f32 v248, v66, v67
	v_cvt_pk_bf16_f32 v249, v68, v69
	v_add_u32_e32 v252, 0x10000, v251
	v_add_u32_e32 v253, 0x18000, v251
	global_store_dwordx4 v252, v[234:237], s[98:99]
	global_store_dwordx4 v252, v[238:241], s[100:101]
	global_store_dwordx4 v253, v[242:245], s[98:99]
	global_store_dwordx4 v253, v[246:249], s[100:101]
	s_waitcnt vmcnt(10)
	v_pk_add_f32 v[62:63], v[62:63], v[142:143]
	v_pk_add_f32 v[64:65], v[64:65], v[144:145]
	v_pk_add_f32 v[54:55], v[54:55], v[130:131]
	v_pk_add_f32 v[56:57], v[56:57], v[132:133]
	v_pk_add_f32 v[58:59], v[58:59], v[146:147]
	v_pk_add_f32 v[60:61], v[60:61], v[148:149]
	v_pk_add_f32 v[50:51], v[50:51], v[134:135]
	v_pk_add_f32 v[52:53], v[52:53], v[136:137]
	v_pk_add_f32 v[46:47], v[46:47], v[142:143]
	v_pk_add_f32 v[48:49], v[48:49], v[144:145]
	v_pk_add_f32 v[38:39], v[38:39], v[130:131]
	v_pk_add_f32 v[40:41], v[40:41], v[132:133]
	v_pk_add_f32 v[42:43], v[42:43], v[146:147]
	v_pk_add_f32 v[44:45], v[44:45], v[148:149]
	v_pk_add_f32 v[34:35], v[34:35], v[134:135]
	v_pk_add_f32 v[36:37], v[36:37], v[136:137]
	v_pk_mul_f32 v[62:63], v[62:63], s[28:29] op_sel_hi:[1,0]
	v_pk_mul_f32 v[64:65], v[64:65], s[28:29] op_sel_hi:[1,0]
	v_pk_mul_f32 v[54:55], v[54:55], s[28:29] op_sel_hi:[1,0]
	v_pk_mul_f32 v[56:57], v[56:57], s[28:29] op_sel_hi:[1,0]
	v_pk_mul_f32 v[58:59], v[58:59], s[28:29] op_sel_hi:[1,0]
	v_pk_mul_f32 v[60:61], v[60:61], s[28:29] op_sel_hi:[1,0]
	v_pk_mul_f32 v[50:51], v[50:51], s[28:29] op_sel_hi:[1,0]
	v_pk_mul_f32 v[52:53], v[52:53], s[28:29] op_sel_hi:[1,0]
	v_pk_mul_f32 v[46:47], v[46:47], s[28:29] op_sel_hi:[1,0]
	v_pk_mul_f32 v[48:49], v[48:49], s[28:29] op_sel_hi:[1,0]
	v_pk_mul_f32 v[38:39], v[38:39], s[28:29] op_sel_hi:[1,0]
	v_pk_mul_f32 v[40:41], v[40:41], s[28:29] op_sel_hi:[1,0]
	v_pk_mul_f32 v[42:43], v[42:43], s[28:29] op_sel_hi:[1,0]
	v_pk_mul_f32 v[44:45], v[44:45], s[28:29] op_sel_hi:[1,0]
	v_pk_mul_f32 v[34:35], v[34:35], s[28:29] op_sel_hi:[1,0]
	v_pk_mul_f32 v[36:37], v[36:37], s[28:29] op_sel_hi:[1,0]
	v_exp_f32_e32 v62, v62
	v_exp_f32_e32 v63, v63
	v_exp_f32_e32 v64, v64
	v_exp_f32_e32 v65, v65
	v_exp_f32_e32 v54, v54
	v_exp_f32_e32 v55, v55
	v_exp_f32_e32 v56, v56
	v_exp_f32_e32 v57, v57
	v_exp_f32_e32 v58, v58
	v_exp_f32_e32 v59, v59
	v_exp_f32_e32 v60, v60
	v_exp_f32_e32 v61, v61
	v_exp_f32_e32 v50, v50
	v_exp_f32_e32 v51, v51
	v_exp_f32_e32 v52, v52
	v_exp_f32_e32 v53, v53
	v_exp_f32_e32 v46, v46
	v_exp_f32_e32 v47, v47
	v_exp_f32_e32 v48, v48
	v_exp_f32_e32 v49, v49
	v_exp_f32_e32 v38, v38
	v_exp_f32_e32 v39, v39
	v_exp_f32_e32 v40, v40
	v_exp_f32_e32 v41, v41
	v_exp_f32_e32 v42, v42
	v_exp_f32_e32 v43, v43
	v_exp_f32_e32 v44, v44
	v_exp_f32_e32 v45, v45
	v_exp_f32_e32 v34, v34
	v_exp_f32_e32 v35, v35
	v_exp_f32_e32 v36, v36
	v_exp_f32_e32 v37, v37
	v_pk_add_f32 v[62:63], v[62:63], 1.0 op_sel_hi:[1,0]
	v_pk_add_f32 v[64:65], v[64:65], 1.0 op_sel_hi:[1,0]
	v_pk_add_f32 v[54:55], v[54:55], 1.0 op_sel_hi:[1,0]
	v_pk_add_f32 v[56:57], v[56:57], 1.0 op_sel_hi:[1,0]
	v_pk_add_f32 v[58:59], v[58:59], 1.0 op_sel_hi:[1,0]
	v_pk_add_f32 v[60:61], v[60:61], 1.0 op_sel_hi:[1,0]
	v_pk_add_f32 v[50:51], v[50:51], 1.0 op_sel_hi:[1,0]
	v_pk_add_f32 v[52:53], v[52:53], 1.0 op_sel_hi:[1,0]
	v_pk_add_f32 v[46:47], v[46:47], 1.0 op_sel_hi:[1,0]
	v_pk_add_f32 v[48:49], v[48:49], 1.0 op_sel_hi:[1,0]
	v_pk_add_f32 v[38:39], v[38:39], 1.0 op_sel_hi:[1,0]
	v_pk_add_f32 v[40:41], v[40:41], 1.0 op_sel_hi:[1,0]
	v_pk_add_f32 v[42:43], v[42:43], 1.0 op_sel_hi:[1,0]
	v_pk_add_f32 v[44:45], v[44:45], 1.0 op_sel_hi:[1,0]
	v_pk_add_f32 v[34:35], v[34:35], 1.0 op_sel_hi:[1,0]
	v_pk_add_f32 v[36:37], v[36:37], 1.0 op_sel_hi:[1,0]
	v_rcp_f32_e32 v62, v62
	v_rcp_f32_e32 v63, v63
	v_rcp_f32_e32 v64, v64
	v_rcp_f32_e32 v65, v65
	v_rcp_f32_e32 v54, v54
	v_rcp_f32_e32 v55, v55
	v_rcp_f32_e32 v56, v56
	v_rcp_f32_e32 v57, v57
	v_rcp_f32_e32 v58, v58
	v_rcp_f32_e32 v59, v59
	v_rcp_f32_e32 v60, v60
	v_rcp_f32_e32 v61, v61
	v_rcp_f32_e32 v50, v50
	v_rcp_f32_e32 v51, v51
	v_rcp_f32_e32 v52, v52
	v_rcp_f32_e32 v53, v53
	v_rcp_f32_e32 v46, v46
	v_rcp_f32_e32 v47, v47
	v_rcp_f32_e32 v48, v48
	v_rcp_f32_e32 v49, v49
	v_rcp_f32_e32 v38, v38
	v_rcp_f32_e32 v39, v39
	v_rcp_f32_e32 v40, v40
	v_rcp_f32_e32 v41, v41
	v_rcp_f32_e32 v42, v42
	v_rcp_f32_e32 v43, v43
	v_rcp_f32_e32 v44, v44
	v_rcp_f32_e32 v45, v45
	v_rcp_f32_e32 v34, v34
	v_rcp_f32_e32 v35, v35
	v_rcp_f32_e32 v36, v36
	v_rcp_f32_e32 v37, v37
	v_lshlrev_b32_e32 v214, 16, v158
	v_and_b32_e32 v215, 0xffff0000, v158
	v_lshlrev_b32_e32 v216, 16, v159
	v_and_b32_e32 v217, 0xffff0000, v159
	v_lshlrev_b32_e32 v218, 16, v160
	v_and_b32_e32 v219, 0xffff0000, v160
	v_lshlrev_b32_e32 v220, 16, v161
	v_and_b32_e32 v221, 0xffff0000, v161
	v_lshlrev_b32_e32 v222, 16, v154
	v_and_b32_e32 v223, 0xffff0000, v154
	v_lshlrev_b32_e32 v224, 16, v155
	v_and_b32_e32 v225, 0xffff0000, v155
	v_lshlrev_b32_e32 v226, 16, v156
	v_and_b32_e32 v227, 0xffff0000, v156
	v_lshlrev_b32_e32 v228, 16, v157
	v_and_b32_e32 v229, 0xffff0000, v157
	v_pk_mul_f32 v[58:59], v[58:59], v[214:215]
	v_pk_mul_f32 v[60:61], v[60:61], v[216:217]
	v_pk_mul_f32 v[50:51], v[50:51], v[218:219]
	v_pk_mul_f32 v[52:53], v[52:53], v[220:221]
	v_pk_mul_f32 v[42:43], v[42:43], v[222:223]
	v_pk_mul_f32 v[44:45], v[44:45], v[224:225]
	v_pk_mul_f32 v[34:35], v[34:35], v[226:227]
	v_pk_mul_f32 v[36:37], v[36:37], v[228:229]
	v_cvt_pk_bf16_f32 v234, v62, v63
	v_cvt_pk_bf16_f32 v235, v64, v65
	v_cvt_pk_bf16_f32 v236, v54, v55
	v_cvt_pk_bf16_f32 v237, v56, v57
	v_cvt_pk_bf16_f32 v238, v58, v59
	v_cvt_pk_bf16_f32 v239, v60, v61
	v_cvt_pk_bf16_f32 v240, v50, v51
	v_cvt_pk_bf16_f32 v241, v52, v53
	v_cvt_pk_bf16_f32 v242, v46, v47
	v_cvt_pk_bf16_f32 v243, v48, v49
	v_cvt_pk_bf16_f32 v244, v38, v39
	v_cvt_pk_bf16_f32 v245, v40, v41
	v_cvt_pk_bf16_f32 v246, v42, v43
	v_cvt_pk_bf16_f32 v247, v44, v45
	v_cvt_pk_bf16_f32 v248, v34, v35
	v_cvt_pk_bf16_f32 v249, v36, v37
	v_add_u32_e32 v252, 0x40000, v251
	v_add_u32_e32 v253, 0x48000, v251
	global_store_dwordx4 v252, v[234:237], s[98:99]
	global_store_dwordx4 v252, v[238:241], s[100:101]
	global_store_dwordx4 v253, v[242:245], s[98:99]
	global_store_dwordx4 v253, v[246:249], s[100:101]
	s_waitcnt vmcnt(12)
	v_pk_add_f32 v[30:31], v[30:31], v[142:143]
	v_pk_add_f32 v[32:33], v[32:33], v[144:145]
	v_pk_add_f32 v[22:23], v[22:23], v[130:131]
	v_pk_add_f32 v[24:25], v[24:25], v[132:133]
	v_pk_add_f32 v[26:27], v[26:27], v[146:147]
	v_pk_add_f32 v[28:29], v[28:29], v[148:149]
	v_pk_add_f32 v[18:19], v[18:19], v[134:135]
	v_pk_add_f32 v[20:21], v[20:21], v[136:137]
	v_pk_add_f32 v[14:15], v[14:15], v[142:143]
	v_pk_add_f32 v[16:17], v[16:17], v[144:145]
	v_pk_add_f32 v[6:7], v[6:7], v[130:131]
	v_pk_add_f32 v[8:9], v[8:9], v[132:133]
	v_pk_add_f32 v[10:11], v[10:11], v[146:147]
	v_pk_add_f32 v[12:13], v[12:13], v[148:149]
	v_pk_add_f32 v[2:3], v[2:3], v[134:135]
	v_pk_add_f32 v[4:5], v[4:5], v[136:137]
	v_pk_mul_f32 v[30:31], v[30:31], s[28:29] op_sel_hi:[1,0]
	v_pk_mul_f32 v[32:33], v[32:33], s[28:29] op_sel_hi:[1,0]
	v_pk_mul_f32 v[22:23], v[22:23], s[28:29] op_sel_hi:[1,0]
	v_pk_mul_f32 v[24:25], v[24:25], s[28:29] op_sel_hi:[1,0]
	v_pk_mul_f32 v[26:27], v[26:27], s[28:29] op_sel_hi:[1,0]
	v_pk_mul_f32 v[28:29], v[28:29], s[28:29] op_sel_hi:[1,0]
	v_pk_mul_f32 v[18:19], v[18:19], s[28:29] op_sel_hi:[1,0]
	v_pk_mul_f32 v[20:21], v[20:21], s[28:29] op_sel_hi:[1,0]
	v_pk_mul_f32 v[14:15], v[14:15], s[28:29] op_sel_hi:[1,0]
	v_pk_mul_f32 v[16:17], v[16:17], s[28:29] op_sel_hi:[1,0]
	v_pk_mul_f32 v[6:7], v[6:7], s[28:29] op_sel_hi:[1,0]
	v_pk_mul_f32 v[8:9], v[8:9], s[28:29] op_sel_hi:[1,0]
	v_pk_mul_f32 v[10:11], v[10:11], s[28:29] op_sel_hi:[1,0]
	v_pk_mul_f32 v[12:13], v[12:13], s[28:29] op_sel_hi:[1,0]
	v_pk_mul_f32 v[2:3], v[2:3], s[28:29] op_sel_hi:[1,0]
	v_pk_mul_f32 v[4:5], v[4:5], s[28:29] op_sel_hi:[1,0]
	v_exp_f32_e32 v30, v30
	v_exp_f32_e32 v31, v31
	v_exp_f32_e32 v32, v32
	v_exp_f32_e32 v33, v33
	v_exp_f32_e32 v22, v22
	v_exp_f32_e32 v23, v23
	v_exp_f32_e32 v24, v24
	v_exp_f32_e32 v25, v25
	v_exp_f32_e32 v26, v26
	v_exp_f32_e32 v27, v27
	v_exp_f32_e32 v28, v28
	v_exp_f32_e32 v29, v29
	v_exp_f32_e32 v18, v18
	v_exp_f32_e32 v19, v19
	v_exp_f32_e32 v20, v20
	v_exp_f32_e32 v21, v21
	v_exp_f32_e32 v14, v14
	v_exp_f32_e32 v15, v15
	v_exp_f32_e32 v16, v16
	v_exp_f32_e32 v17, v17
	v_exp_f32_e32 v6, v6
	v_exp_f32_e32 v7, v7
	v_exp_f32_e32 v8, v8
	v_exp_f32_e32 v9, v9
	v_exp_f32_e32 v10, v10
	v_exp_f32_e32 v11, v11
	v_exp_f32_e32 v12, v12
	v_exp_f32_e32 v13, v13
	v_exp_f32_e32 v2, v2
	v_exp_f32_e32 v3, v3
	v_exp_f32_e32 v4, v4
	v_exp_f32_e32 v5, v5
	v_pk_add_f32 v[30:31], v[30:31], 1.0 op_sel_hi:[1,0]
	v_pk_add_f32 v[32:33], v[32:33], 1.0 op_sel_hi:[1,0]
	v_pk_add_f32 v[22:23], v[22:23], 1.0 op_sel_hi:[1,0]
	v_pk_add_f32 v[24:25], v[24:25], 1.0 op_sel_hi:[1,0]
	v_pk_add_f32 v[26:27], v[26:27], 1.0 op_sel_hi:[1,0]
	v_pk_add_f32 v[28:29], v[28:29], 1.0 op_sel_hi:[1,0]
	v_pk_add_f32 v[18:19], v[18:19], 1.0 op_sel_hi:[1,0]
	v_pk_add_f32 v[20:21], v[20:21], 1.0 op_sel_hi:[1,0]
	v_pk_add_f32 v[14:15], v[14:15], 1.0 op_sel_hi:[1,0]
	v_pk_add_f32 v[16:17], v[16:17], 1.0 op_sel_hi:[1,0]
	v_pk_add_f32 v[6:7], v[6:7], 1.0 op_sel_hi:[1,0]
	v_pk_add_f32 v[8:9], v[8:9], 1.0 op_sel_hi:[1,0]
	v_pk_add_f32 v[10:11], v[10:11], 1.0 op_sel_hi:[1,0]
	v_pk_add_f32 v[12:13], v[12:13], 1.0 op_sel_hi:[1,0]
	v_pk_add_f32 v[2:3], v[2:3], 1.0 op_sel_hi:[1,0]
	v_pk_add_f32 v[4:5], v[4:5], 1.0 op_sel_hi:[1,0]
	v_rcp_f32_e32 v30, v30
	v_rcp_f32_e32 v31, v31
	v_rcp_f32_e32 v32, v32
	v_rcp_f32_e32 v33, v33
	v_rcp_f32_e32 v22, v22
	v_rcp_f32_e32 v23, v23
	v_rcp_f32_e32 v24, v24
	v_rcp_f32_e32 v25, v25
	v_rcp_f32_e32 v26, v26
	v_rcp_f32_e32 v27, v27
	v_rcp_f32_e32 v28, v28
	v_rcp_f32_e32 v29, v29
	v_rcp_f32_e32 v18, v18
	v_rcp_f32_e32 v19, v19
	v_rcp_f32_e32 v20, v20
	v_rcp_f32_e32 v21, v21
	v_rcp_f32_e32 v14, v14
	v_rcp_f32_e32 v15, v15
	v_rcp_f32_e32 v16, v16
	v_rcp_f32_e32 v17, v17
	v_rcp_f32_e32 v6, v6
	v_rcp_f32_e32 v7, v7
	v_rcp_f32_e32 v8, v8
	v_rcp_f32_e32 v9, v9
	v_rcp_f32_e32 v10, v10
	v_rcp_f32_e32 v11, v11
	v_rcp_f32_e32 v12, v12
	v_rcp_f32_e32 v13, v13
	v_rcp_f32_e32 v2, v2
	v_rcp_f32_e32 v3, v3
	v_rcp_f32_e32 v4, v4
	v_rcp_f32_e32 v5, v5
	v_lshlrev_b32_e32 v214, 16, v150
	v_and_b32_e32 v215, 0xffff0000, v150
	v_lshlrev_b32_e32 v216, 16, v151
	v_and_b32_e32 v217, 0xffff0000, v151
	v_lshlrev_b32_e32 v218, 16, v152
	v_and_b32_e32 v219, 0xffff0000, v152
	v_lshlrev_b32_e32 v220, 16, v153
	v_and_b32_e32 v221, 0xffff0000, v153
	v_lshlrev_b32_e32 v222, 16, v138
	v_and_b32_e32 v223, 0xffff0000, v138
	v_lshlrev_b32_e32 v224, 16, v139
	v_and_b32_e32 v225, 0xffff0000, v139
	v_lshlrev_b32_e32 v226, 16, v140
	v_and_b32_e32 v227, 0xffff0000, v140
	v_lshlrev_b32_e32 v228, 16, v141
	v_and_b32_e32 v229, 0xffff0000, v141
	v_pk_mul_f32 v[26:27], v[26:27], v[214:215]
	v_pk_mul_f32 v[28:29], v[28:29], v[216:217]
	v_pk_mul_f32 v[18:19], v[18:19], v[218:219]
	v_pk_mul_f32 v[20:21], v[20:21], v[220:221]
	v_pk_mul_f32 v[10:11], v[10:11], v[222:223]
	v_pk_mul_f32 v[12:13], v[12:13], v[224:225]
	v_pk_mul_f32 v[2:3], v[2:3], v[226:227]
	v_pk_mul_f32 v[4:5], v[4:5], v[228:229]
	v_cvt_pk_bf16_f32 v234, v30, v31
	v_cvt_pk_bf16_f32 v235, v32, v33
	v_cvt_pk_bf16_f32 v236, v22, v23
	v_cvt_pk_bf16_f32 v237, v24, v25
	v_cvt_pk_bf16_f32 v238, v26, v27
	v_cvt_pk_bf16_f32 v239, v28, v29
	v_cvt_pk_bf16_f32 v240, v18, v19
	v_cvt_pk_bf16_f32 v241, v20, v21
	v_cvt_pk_bf16_f32 v242, v14, v15
	v_cvt_pk_bf16_f32 v243, v16, v17
	v_cvt_pk_bf16_f32 v244, v6, v7
	v_cvt_pk_bf16_f32 v245, v8, v9
	v_cvt_pk_bf16_f32 v246, v10, v11
	v_cvt_pk_bf16_f32 v247, v12, v13
	v_cvt_pk_bf16_f32 v248, v2, v3
	v_cvt_pk_bf16_f32 v249, v4, v5
	v_add_u32_e32 v252, 0x50000, v251
	v_add_u32_e32 v253, 0x58000, v251
	global_store_dwordx4 v252, v[234:237], s[98:99]
	global_store_dwordx4 v252, v[238:241], s[100:101]
	global_store_dwordx4 v253, v[242:245], s[98:99]
	global_store_dwordx4 v253, v[246:249], s[100:101]
	s_andn2_b64 vcc, exec, s[2:3]
	s_mov_b64 s[2:3], -1
	s_cbranch_vccnz .LBB0_632
	s_andn2_b64 vcc, exec, s[14:15]
	s_cbranch_vccnz .LBB0_631
	s_barrier
	s_branch .LBB0_631
